# base_sc1
# baseline (speedup 1.0000x reference)
.LBB0_7:
	s_or_b64 exec, exec, s[0:1]
	s_waitcnt lgkmcnt(0)
	s_barrier
	ds_read_b128 v[0:3], v30
	s_add_u32 s0, s6, s4
	s_addc_u32 s1, s7, s5
	v_add_u32_e32 v14, v15, v14
	ds_read_b128 v[4:7], v14 offset:16384
	s_waitcnt lgkmcnt(1)
	global_store_dwordx4 v30, v[0:3], s[0:1] sc1
	ds_read_b128 v[0:3], v14 offset:4096
	v_lshl_add_u64 v[16:17], s[0:1], 0, v[30:31]
	v_add_co_u32_e32 v12, vcc, 0x1000, v16
	ds_read_b128 v[8:11], v49
	s_nop 0
	v_addc_co_u32_e32 v13, vcc, 0, v17, vcc
	s_waitcnt lgkmcnt(1)
	global_store_dwordx4 v[12:13], v[0:3], off sc1
	ds_read_b128 v[0:3], v14 offset:8192
	ds_read_b128 v[12:15], v14 offset:12288
	v_add_co_u32_e32 v18, vcc, 0x2000, v16
	s_nop 1
	v_addc_co_u32_e32 v19, vcc, 0, v17, vcc
	s_waitcnt lgkmcnt(1)
	global_store_dwordx4 v[18:19], v[0:3], off sc1
	s_nop 1
	v_add_co_u32_e32 v0, vcc, 0x3000, v16
	s_nop 1
	v_addc_co_u32_e32 v1, vcc, 0, v17, vcc
	s_waitcnt lgkmcnt(0)
	global_store_dwordx4 v[0:1], v[12:15], off sc1
	v_lshlrev_b32_e32 v0, 4, v48
	global_store_dwordx4 v0, v[4:7], s[0:1] sc1
	global_store_dwordx4 v49, v[8:11], s[0:1] sc1
	s_endpgm
